# P1/P3 K-loops: 8 of 16 LDS-DMA per loop take SGPR base + 32-bit lane offset (saddr form), VALU 64-bit adds removed
# baseline (speedup 1.0000x reference)
.LBB0_105:
	ds_read_b128 v[146:149], v160
	ds_read_b128 v[164:167], v160 offset:1024
	ds_read_b128 v[168:171], v151
	ds_read_b128 v[172:175], v152
	ds_read_b128 v[176:179], v161
	ds_read_b128 v[180:183], v161 offset:1024
	ds_read_b128 v[184:187], v153
	ds_read_b128 v[188:191], v154
	s_add_u32 s40, s38, 0xfffc0080
	s_addc_u32 s41, s39, -1
	s_cmp_eq_u32 s84, 12
	s_cselect_b32 s43, s29, s41
	s_cselect_b32 s42, s80, s40
	s_cselect_b32 s41, s27, s83
	s_cselect_b32 s40, s81, s82
	s_add_i32 m0, s48, 0xc000
	ds_read_b128 v[192:195], v162
	ds_read_b128 v[196:199], v162 offset:1024
	ds_read_b128 v[200:203], v162 offset:2048
	ds_read_b128 v[204:207], v162 offset:3072
	ds_read_b128 v[208:211], v162 offset:4096
	ds_read_b128 v[212:215], v162 offset:5120
	ds_read_b128 v[216:219], v162 offset:6144
	ds_read_b128 v[220:223], v162 offset:7168
	global_load_lds_dwordx4 v136, s[38:39]
	s_add_i32 m0, s48, 0xe000
	s_nop 0
	global_load_lds_dwordx4 v138, s[38:39]
	s_waitcnt vmcnt(8)
	s_waitcnt lgkmcnt(0)
	s_barrier
	s_setprio 1
	s_waitcnt lgkmcnt(0)
	v_mfma_f32_16x16x32_bf16 v[124:127], v[146:149], v[192:195], v[124:127]
	v_mfma_f32_16x16x32_bf16 v[120:123], v[168:171], v[192:195], v[120:123]
	v_mfma_f32_16x16x32_bf16 v[112:115], v[146:149], v[200:203], v[112:115]
	v_mfma_f32_16x16x32_bf16 v[104:107], v[168:171], v[200:203], v[104:107]
	v_mfma_f32_16x16x32_bf16 v[96:99], v[146:149], v[208:211], v[96:99]
	v_mfma_f32_16x16x32_bf16 v[88:91], v[168:171], v[208:211], v[88:91]
	v_mfma_f32_16x16x32_bf16 v[80:83], v[146:149], v[216:219], v[80:83]
	v_mfma_f32_16x16x32_bf16 v[72:75], v[168:171], v[216:219], v[72:75]
	v_mfma_f32_16x16x32_bf16 v[124:127], v[164:167], v[196:199], v[124:127]
	v_mfma_f32_16x16x32_bf16 v[120:123], v[172:175], v[196:199], v[120:123]
	v_mfma_f32_16x16x32_bf16 v[112:115], v[164:167], v[204:207], v[112:115]
	v_mfma_f32_16x16x32_bf16 v[104:107], v[172:175], v[204:207], v[104:107]
	v_mfma_f32_16x16x32_bf16 v[96:99], v[164:167], v[212:215], v[96:99]
	v_mfma_f32_16x16x32_bf16 v[88:91], v[172:175], v[212:215], v[88:91]
	v_mfma_f32_16x16x32_bf16 v[80:83], v[164:167], v[220:223], v[80:83]
	v_mfma_f32_16x16x32_bf16 v[72:75], v[172:175], v[220:223], v[72:75]
	s_setprio 0
	s_setprio 1
	v_mfma_f32_16x16x32_bf16 v[116:119], v[176:179], v[192:195], v[116:119]
	v_mfma_f32_16x16x32_bf16 v[108:111], v[184:187], v[192:195], v[108:111]
	v_mfma_f32_16x16x32_bf16 v[100:103], v[176:179], v[200:203], v[100:103]
	v_mfma_f32_16x16x32_bf16 v[92:95], v[184:187], v[200:203], v[92:95]
	v_mfma_f32_16x16x32_bf16 v[84:87], v[176:179], v[208:211], v[84:87]
	v_mfma_f32_16x16x32_bf16 v[76:79], v[184:187], v[208:211], v[76:79]
	v_mfma_f32_16x16x32_bf16 v[68:71], v[176:179], v[216:219], v[68:71]
	v_mfma_f32_16x16x32_bf16 v[64:67], v[184:187], v[216:219], v[64:67]
	v_mfma_f32_16x16x32_bf16 v[116:119], v[180:183], v[196:199], v[116:119]
	v_mfma_f32_16x16x32_bf16 v[108:111], v[188:191], v[196:199], v[108:111]
	v_mfma_f32_16x16x32_bf16 v[100:103], v[180:183], v[204:207], v[100:103]
	v_mfma_f32_16x16x32_bf16 v[92:95], v[188:191], v[204:207], v[92:95]
	v_mfma_f32_16x16x32_bf16 v[84:87], v[180:183], v[212:215], v[84:87]
	v_mfma_f32_16x16x32_bf16 v[76:79], v[188:191], v[212:215], v[76:79]
	v_mfma_f32_16x16x32_bf16 v[68:71], v[180:183], v[220:223], v[68:71]
	v_mfma_f32_16x16x32_bf16 v[64:67], v[188:191], v[220:223], v[64:67]
	s_setprio 0
	s_barrier
	s_add_i32 m0, s76, s47
	v_lshl_add_u64 v[224:225], s[40:41], 0, v[132:133]
	s_add_u32 s86, s40, 0x40000
	ds_read_b128 v[192:195], v162 offset:16384
	ds_read_b128 v[196:199], v162 offset:17408
	ds_read_b128 v[200:203], v162 offset:18432
	ds_read_b128 v[204:207], v162 offset:19456
	ds_read_b128 v[208:211], v162 offset:20480
	ds_read_b128 v[212:215], v162 offset:21504
	ds_read_b128 v[216:219], v162 offset:22528
	ds_read_b128 v[220:223], v162 offset:23552
	global_load_lds_dwordx4 v[224:225], off
	v_lshl_add_u64 v[226:227], s[40:41], 0, v[128:129]
	s_mov_b32 m0, s37
	s_addc_u32 s87, s41, 0
	global_load_lds_dwordx4 v[226:227], off
	s_add_i32 m0, s77, s47
	v_lshl_add_u64 v[230:231], s[42:43], 0, v[130:131]
	s_nop 1
	global_load_lds_dwordx4 v132, s[86:87]
	s_mov_b32 m0, s57
	s_nop 0
	global_load_lds_dwordx4 v128, s[86:87]
	v_lshl_add_u64 v[228:229], s[42:43], 0, v[134:135]
	s_mov_b32 m0, s48
	s_nop 0
	global_load_lds_dwordx4 v[228:229], off
	s_mov_b32 m0, s58
	s_nop 0
	global_load_lds_dwordx4 v[230:231], off
	s_waitcnt vmcnt(8)
	s_waitcnt lgkmcnt(0)
	s_barrier
	s_setprio 1
	s_waitcnt lgkmcnt(0)
	v_mfma_f32_16x16x32_bf16 v[60:63], v[146:149], v[192:195], v[60:63]
	v_mfma_f32_16x16x32_bf16 v[56:59], v[168:171], v[192:195], v[56:59]
	v_mfma_f32_16x16x32_bf16 v[48:51], v[146:149], v[200:203], v[48:51]
	v_mfma_f32_16x16x32_bf16 v[40:43], v[168:171], v[200:203], v[40:43]
	v_mfma_f32_16x16x32_bf16 v[32:35], v[146:149], v[208:211], v[32:35]
	v_mfma_f32_16x16x32_bf16 v[24:27], v[168:171], v[208:211], v[24:27]
	v_mfma_f32_16x16x32_bf16 v[16:19], v[146:149], v[216:219], v[16:19]
	v_mfma_f32_16x16x32_bf16 v[8:11], v[168:171], v[216:219], v[8:11]
	v_mfma_f32_16x16x32_bf16 v[60:63], v[164:167], v[196:199], v[60:63]
	v_mfma_f32_16x16x32_bf16 v[56:59], v[172:175], v[196:199], v[56:59]
	v_mfma_f32_16x16x32_bf16 v[48:51], v[164:167], v[204:207], v[48:51]
	v_mfma_f32_16x16x32_bf16 v[40:43], v[172:175], v[204:207], v[40:43]
	v_mfma_f32_16x16x32_bf16 v[32:35], v[164:167], v[212:215], v[32:35]
	v_mfma_f32_16x16x32_bf16 v[24:27], v[172:175], v[212:215], v[24:27]
	v_mfma_f32_16x16x32_bf16 v[16:19], v[164:167], v[220:223], v[16:19]
	v_mfma_f32_16x16x32_bf16 v[8:11], v[172:175], v[220:223], v[8:11]
	s_setprio 0
	s_setprio 1
	v_mfma_f32_16x16x32_bf16 v[52:55], v[176:179], v[192:195], v[52:55]
	v_mfma_f32_16x16x32_bf16 v[44:47], v[184:187], v[192:195], v[44:47]
	v_mfma_f32_16x16x32_bf16 v[36:39], v[176:179], v[200:203], v[36:39]
	v_mfma_f32_16x16x32_bf16 v[28:31], v[184:187], v[200:203], v[28:31]
	v_mfma_f32_16x16x32_bf16 v[20:23], v[176:179], v[208:211], v[20:23]
	v_mfma_f32_16x16x32_bf16 v[12:15], v[184:187], v[208:211], v[12:15]
	v_mfma_f32_16x16x32_bf16 v[4:7], v[176:179], v[216:219], v[4:7]
	v_mfma_f32_16x16x32_bf16 v[0:3], v[184:187], v[216:219], v[0:3]
	v_mfma_f32_16x16x32_bf16 v[52:55], v[180:183], v[196:199], v[52:55]
	v_mfma_f32_16x16x32_bf16 v[44:47], v[188:191], v[196:199], v[44:47]
	v_mfma_f32_16x16x32_bf16 v[36:39], v[180:183], v[204:207], v[36:39]
	v_mfma_f32_16x16x32_bf16 v[28:31], v[188:191], v[204:207], v[28:31]
	v_mfma_f32_16x16x32_bf16 v[20:23], v[180:183], v[212:215], v[20:23]
	v_mfma_f32_16x16x32_bf16 v[12:15], v[188:191], v[212:215], v[12:15]
	v_mfma_f32_16x16x32_bf16 v[4:7], v[180:183], v[220:223], v[4:7]
	v_mfma_f32_16x16x32_bf16 v[0:3], v[188:191], v[220:223], v[0:3]
	s_setprio 0
	s_barrier
	s_add_i32 s85, 0, 0x18000
	v_add_u32_e32 v144, s85, v150
	s_add_i32 s86, 0, 0x1c000
	ds_read_b128 v[146:149], v144
	ds_read_b128 v[164:167], v144 offset:1024
	ds_read_b128 v[168:171], v155
	ds_read_b128 v[172:175], v156
	v_add_u32_e32 v144, s86, v150
	ds_read_b128 v[176:179], v144
	ds_read_b128 v[180:183], v144 offset:1024
	ds_read_b128 v[184:187], v157
	ds_read_b128 v[188:191], v158
	s_add_u32 s42, s42, 0x40000
	s_addc_u32 s43, s43, 0
	s_mov_b32 m0, s59
	ds_read_b128 v[192:195], v162 offset:32768
	ds_read_b128 v[196:199], v162 offset:33792
	ds_read_b128 v[200:203], v162 offset:34816
	ds_read_b128 v[204:207], v162 offset:35840
	ds_read_b128 v[208:211], v162 offset:36864
	ds_read_b128 v[212:215], v162 offset:37888
	ds_read_b128 v[216:219], v162 offset:38912
	ds_read_b128 v[220:223], v162 offset:39936
	global_load_lds_dwordx4 v134, s[42:43]
	s_mov_b32 m0, s60
	s_nop 0
	global_load_lds_dwordx4 v130, s[42:43]
	s_waitcnt vmcnt(8)
	s_waitcnt lgkmcnt(0)
	s_barrier
	s_setprio 1
	s_waitcnt lgkmcnt(0)
	v_mfma_f32_16x16x32_bf16 v[124:127], v[146:149], v[192:195], v[124:127]
	v_mfma_f32_16x16x32_bf16 v[120:123], v[168:171], v[192:195], v[120:123]
	v_mfma_f32_16x16x32_bf16 v[112:115], v[146:149], v[200:203], v[112:115]
	v_mfma_f32_16x16x32_bf16 v[104:107], v[168:171], v[200:203], v[104:107]
	v_mfma_f32_16x16x32_bf16 v[96:99], v[146:149], v[208:211], v[96:99]
	v_mfma_f32_16x16x32_bf16 v[88:91], v[168:171], v[208:211], v[88:91]
	v_mfma_f32_16x16x32_bf16 v[80:83], v[146:149], v[216:219], v[80:83]
	v_mfma_f32_16x16x32_bf16 v[72:75], v[168:171], v[216:219], v[72:75]
	v_mfma_f32_16x16x32_bf16 v[124:127], v[164:167], v[196:199], v[124:127]
	v_mfma_f32_16x16x32_bf16 v[120:123], v[172:175], v[196:199], v[120:123]
	v_mfma_f32_16x16x32_bf16 v[112:115], v[164:167], v[204:207], v[112:115]
	v_mfma_f32_16x16x32_bf16 v[104:107], v[172:175], v[204:207], v[104:107]
	v_mfma_f32_16x16x32_bf16 v[96:99], v[164:167], v[212:215], v[96:99]
	v_mfma_f32_16x16x32_bf16 v[88:91], v[172:175], v[212:215], v[88:91]
	v_mfma_f32_16x16x32_bf16 v[80:83], v[164:167], v[220:223], v[80:83]
	v_mfma_f32_16x16x32_bf16 v[72:75], v[172:175], v[220:223], v[72:75]
	s_setprio 0
	s_setprio 1
	v_mfma_f32_16x16x32_bf16 v[116:119], v[176:179], v[192:195], v[116:119]
	v_mfma_f32_16x16x32_bf16 v[108:111], v[184:187], v[192:195], v[108:111]
	v_mfma_f32_16x16x32_bf16 v[100:103], v[176:179], v[200:203], v[100:103]
	v_mfma_f32_16x16x32_bf16 v[92:95], v[184:187], v[200:203], v[92:95]
	v_mfma_f32_16x16x32_bf16 v[84:87], v[176:179], v[208:211], v[84:87]
	v_mfma_f32_16x16x32_bf16 v[76:79], v[184:187], v[208:211], v[76:79]
	v_mfma_f32_16x16x32_bf16 v[68:71], v[176:179], v[216:219], v[68:71]
	v_mfma_f32_16x16x32_bf16 v[64:67], v[184:187], v[216:219], v[64:67]
	v_mfma_f32_16x16x32_bf16 v[116:119], v[180:183], v[196:199], v[116:119]
	v_mfma_f32_16x16x32_bf16 v[108:111], v[188:191], v[196:199], v[108:111]
	v_mfma_f32_16x16x32_bf16 v[100:103], v[180:183], v[204:207], v[100:103]
	v_mfma_f32_16x16x32_bf16 v[92:95], v[188:191], v[204:207], v[92:95]
	v_mfma_f32_16x16x32_bf16 v[84:87], v[180:183], v[212:215], v[84:87]
	v_mfma_f32_16x16x32_bf16 v[76:79], v[188:191], v[212:215], v[76:79]
	v_mfma_f32_16x16x32_bf16 v[68:71], v[180:183], v[220:223], v[68:71]
	v_mfma_f32_16x16x32_bf16 v[64:67], v[188:191], v[220:223], v[64:67]
	s_setprio 0
	s_barrier
	s_add_i32 m0, s85, s47
	v_lshl_add_u64 v[224:225], v[224:225], 0, s[24:25]
	s_add_u32 s40, s40, 0x40080
	ds_read_b128 v[192:195], v162 offset:49152
	ds_read_b128 v[196:199], v162 offset:50176
	ds_read_b128 v[200:203], v162 offset:51200
	ds_read_b128 v[204:207], v162 offset:52224
	ds_read_b128 v[208:211], v162 offset:53248
	ds_read_b128 v[212:215], v162 offset:54272
	ds_read_b128 v[216:219], v162 offset:55296
	ds_read_b128 v[220:223], v162 offset:56320
	global_load_lds_dwordx4 v[224:225], off
	v_lshl_add_u64 v[224:225], v[226:227], 0, s[24:25]
	s_mov_b32 m0, s71
	s_addc_u32 s41, s41, 0
	global_load_lds_dwordx4 v[224:225], off
	s_add_i32 m0, s86, s47
	s_nop 0
	s_nop 1
	global_load_lds_dwordx4 v132, s[40:41]
	s_mov_b32 m0, s72
	s_nop 0
	global_load_lds_dwordx4 v128, s[40:41]
	v_lshl_add_u64 v[224:225], v[228:229], 0, s[24:25]
	s_mov_b32 m0, s74
	s_nop 0
	global_load_lds_dwordx4 v[224:225], off
	v_lshl_add_u64 v[224:225], v[230:231], 0, s[24:25]
	s_mov_b32 m0, s75
	s_nop 0
	global_load_lds_dwordx4 v[224:225], off
	s_waitcnt vmcnt(8)
	s_waitcnt lgkmcnt(0)
	s_barrier
	s_setprio 1
	s_waitcnt lgkmcnt(0)
	v_mfma_f32_16x16x32_bf16 v[60:63], v[146:149], v[192:195], v[60:63]
	v_mfma_f32_16x16x32_bf16 v[56:59], v[168:171], v[192:195], v[56:59]
	v_mfma_f32_16x16x32_bf16 v[48:51], v[146:149], v[200:203], v[48:51]
	v_mfma_f32_16x16x32_bf16 v[40:43], v[168:171], v[200:203], v[40:43]
	v_mfma_f32_16x16x32_bf16 v[32:35], v[146:149], v[208:211], v[32:35]
	v_mfma_f32_16x16x32_bf16 v[24:27], v[168:171], v[208:211], v[24:27]
	v_mfma_f32_16x16x32_bf16 v[16:19], v[146:149], v[216:219], v[16:19]
	v_mfma_f32_16x16x32_bf16 v[8:11], v[168:171], v[216:219], v[8:11]
	v_mfma_f32_16x16x32_bf16 v[60:63], v[164:167], v[196:199], v[60:63]
	v_mfma_f32_16x16x32_bf16 v[56:59], v[172:175], v[196:199], v[56:59]
	v_mfma_f32_16x16x32_bf16 v[48:51], v[164:167], v[204:207], v[48:51]
	v_mfma_f32_16x16x32_bf16 v[40:43], v[172:175], v[204:207], v[40:43]
	v_mfma_f32_16x16x32_bf16 v[32:35], v[164:167], v[212:215], v[32:35]
	v_mfma_f32_16x16x32_bf16 v[24:27], v[172:175], v[212:215], v[24:27]
	v_mfma_f32_16x16x32_bf16 v[16:19], v[164:167], v[220:223], v[16:19]
	v_mfma_f32_16x16x32_bf16 v[8:11], v[172:175], v[220:223], v[8:11]
	s_setprio 0
	s_setprio 1
	v_mfma_f32_16x16x32_bf16 v[52:55], v[176:179], v[192:195], v[52:55]
	v_mfma_f32_16x16x32_bf16 v[44:47], v[184:187], v[192:195], v[44:47]
	v_mfma_f32_16x16x32_bf16 v[36:39], v[176:179], v[200:203], v[36:39]
	v_mfma_f32_16x16x32_bf16 v[28:31], v[184:187], v[200:203], v[28:31]
	v_mfma_f32_16x16x32_bf16 v[20:23], v[176:179], v[208:211], v[20:23]
	v_mfma_f32_16x16x32_bf16 v[12:15], v[184:187], v[208:211], v[12:15]
	v_mfma_f32_16x16x32_bf16 v[4:7], v[176:179], v[216:219], v[4:7]
	v_mfma_f32_16x16x32_bf16 v[0:3], v[184:187], v[216:219], v[0:3]
	v_mfma_f32_16x16x32_bf16 v[52:55], v[180:183], v[196:199], v[52:55]
	v_mfma_f32_16x16x32_bf16 v[44:47], v[188:191], v[196:199], v[44:47]
	v_mfma_f32_16x16x32_bf16 v[36:39], v[180:183], v[204:207], v[36:39]
	v_mfma_f32_16x16x32_bf16 v[28:31], v[188:191], v[204:207], v[28:31]
	v_mfma_f32_16x16x32_bf16 v[20:23], v[180:183], v[212:215], v[20:23]
	v_mfma_f32_16x16x32_bf16 v[12:15], v[188:191], v[212:215], v[12:15]
	v_mfma_f32_16x16x32_bf16 v[4:7], v[180:183], v[220:223], v[4:7]
	v_mfma_f32_16x16x32_bf16 v[0:3], v[188:191], v[220:223], v[0:3]
	s_setprio 0
	s_barrier
	s_add_i32 s84, s84, 2
	s_add_u32 s38, s38, 0x100
	s_addc_u32 s39, s39, 0
	s_add_u32 s82, s82, 0x100
	s_addc_u32 s83, s83, 0
	s_cmp_gt_u32 s84, 13
	s_cbranch_scc0 .LBB0_105
	s_and_b64 vcc, exec, s[12:13]
	s_cbranch_vccz .LBB0_108
	s_barrier

.LBB0_409:
	ds_read_b128 v[144:147], v159
	ds_read_b128 v[162:165], v159 offset:1024
	ds_read_b128 v[166:169], v150
	ds_read_b128 v[170:173], v151
	ds_read_b128 v[174:177], v160
	ds_read_b128 v[178:181], v160 offset:1024
	ds_read_b128 v[182:185], v152
	ds_read_b128 v[186:189], v153
	s_add_u32 s28, s26, 0xfffc0080
	s_addc_u32 s29, s27, -1
	s_cmp_eq_u32 s61, 12
	s_cselect_b32 s31, s19, s29
	s_cselect_b32 s30, s57, s28
	s_cselect_b32 s29, s17, s60
	s_cselect_b32 s28, s58, s59
	s_add_i32 m0, s38, 0xc000
	ds_read_b128 v[190:193], v161
	ds_read_b128 v[194:197], v161 offset:1024
	ds_read_b128 v[198:201], v161 offset:2048
	ds_read_b128 v[202:205], v161 offset:3072
	ds_read_b128 v[206:209], v161 offset:4096
	ds_read_b128 v[210:213], v161 offset:5120
	ds_read_b128 v[214:217], v161 offset:6144
	ds_read_b128 v[218:221], v161 offset:7168
	global_load_lds_dwordx4 v136, s[26:27]
	s_add_i32 m0, s38, 0xe000
	s_nop 0
	global_load_lds_dwordx4 v138, s[26:27]
	s_waitcnt vmcnt(8)
	s_waitcnt lgkmcnt(0)
	s_barrier
	s_setprio 1
	s_waitcnt lgkmcnt(0)
	v_mfma_f32_16x16x32_bf16 v[124:127], v[144:147], v[190:193], v[124:127]
	v_mfma_f32_16x16x32_bf16 v[120:123], v[166:169], v[190:193], v[120:123]
	v_mfma_f32_16x16x32_bf16 v[108:111], v[144:147], v[198:201], v[108:111]
	v_mfma_f32_16x16x32_bf16 v[104:107], v[166:169], v[198:201], v[104:107]
	v_mfma_f32_16x16x32_bf16 v[92:95], v[144:147], v[206:209], v[92:95]
	v_mfma_f32_16x16x32_bf16 v[88:91], v[166:169], v[206:209], v[88:91]
	v_mfma_f32_16x16x32_bf16 v[76:79], v[144:147], v[214:217], v[76:79]
	v_mfma_f32_16x16x32_bf16 v[72:75], v[166:169], v[214:217], v[72:75]
	v_mfma_f32_16x16x32_bf16 v[124:127], v[162:165], v[194:197], v[124:127]
	v_mfma_f32_16x16x32_bf16 v[120:123], v[170:173], v[194:197], v[120:123]
	v_mfma_f32_16x16x32_bf16 v[108:111], v[162:165], v[202:205], v[108:111]
	v_mfma_f32_16x16x32_bf16 v[104:107], v[170:173], v[202:205], v[104:107]
	v_mfma_f32_16x16x32_bf16 v[92:95], v[162:165], v[210:213], v[92:95]
	v_mfma_f32_16x16x32_bf16 v[88:91], v[170:173], v[210:213], v[88:91]
	v_mfma_f32_16x16x32_bf16 v[76:79], v[162:165], v[218:221], v[76:79]
	v_mfma_f32_16x16x32_bf16 v[72:75], v[170:173], v[218:221], v[72:75]
	s_setprio 0
	s_setprio 1
	v_mfma_f32_16x16x32_bf16 v[116:119], v[174:177], v[190:193], v[116:119]
	v_mfma_f32_16x16x32_bf16 v[112:115], v[182:185], v[190:193], v[112:115]
	v_mfma_f32_16x16x32_bf16 v[100:103], v[174:177], v[198:201], v[100:103]
	v_mfma_f32_16x16x32_bf16 v[96:99], v[182:185], v[198:201], v[96:99]
	v_mfma_f32_16x16x32_bf16 v[84:87], v[174:177], v[206:209], v[84:87]
	v_mfma_f32_16x16x32_bf16 v[80:83], v[182:185], v[206:209], v[80:83]
	v_mfma_f32_16x16x32_bf16 v[68:71], v[174:177], v[214:217], v[68:71]
	v_mfma_f32_16x16x32_bf16 v[64:67], v[182:185], v[214:217], v[64:67]
	v_mfma_f32_16x16x32_bf16 v[116:119], v[178:181], v[194:197], v[116:119]
	v_mfma_f32_16x16x32_bf16 v[112:115], v[186:189], v[194:197], v[112:115]
	v_mfma_f32_16x16x32_bf16 v[100:103], v[178:181], v[202:205], v[100:103]
	v_mfma_f32_16x16x32_bf16 v[96:99], v[186:189], v[202:205], v[96:99]
	v_mfma_f32_16x16x32_bf16 v[84:87], v[178:181], v[210:213], v[84:87]
	v_mfma_f32_16x16x32_bf16 v[80:83], v[186:189], v[210:213], v[80:83]
	v_mfma_f32_16x16x32_bf16 v[68:71], v[178:181], v[218:221], v[68:71]
	v_mfma_f32_16x16x32_bf16 v[64:67], v[186:189], v[218:221], v[64:67]
	s_setprio 0
	s_barrier
	s_add_i32 m0, s50, s37
	v_lshl_add_u64 v[222:223], s[28:29], 0, v[132:133]
	s_add_u32 s70, s28, 0x40000
	ds_read_b128 v[190:193], v161 offset:16384
	ds_read_b128 v[194:197], v161 offset:17408
	ds_read_b128 v[198:201], v161 offset:18432
	ds_read_b128 v[202:205], v161 offset:19456
	ds_read_b128 v[206:209], v161 offset:20480
	ds_read_b128 v[210:213], v161 offset:21504
	ds_read_b128 v[214:217], v161 offset:22528
	ds_read_b128 v[218:221], v161 offset:23552
	global_load_lds_dwordx4 v[222:223], off
	v_lshl_add_u64 v[224:225], s[28:29], 0, v[128:129]
	s_mov_b32 m0, s25
	s_addc_u32 s71, s29, 0
	global_load_lds_dwordx4 v[224:225], off
	s_add_i32 m0, s51, s37
	v_lshl_add_u64 v[228:229], s[30:31], 0, v[130:131]
	s_nop 1
	global_load_lds_dwordx4 v132, s[70:71]
	s_mov_b32 m0, s40
	s_nop 0
	global_load_lds_dwordx4 v128, s[70:71]
	v_lshl_add_u64 v[226:227], s[30:31], 0, v[134:135]
	s_mov_b32 m0, s38
	s_nop 0
	global_load_lds_dwordx4 v[226:227], off
	s_mov_b32 m0, s41
	s_nop 0
	global_load_lds_dwordx4 v[228:229], off
	s_waitcnt vmcnt(8)
	s_waitcnt lgkmcnt(0)
	s_barrier
	s_setprio 1
	s_waitcnt lgkmcnt(0)
	v_mfma_f32_16x16x32_bf16 v[60:63], v[144:147], v[190:193], v[60:63]
	v_mfma_f32_16x16x32_bf16 v[56:59], v[166:169], v[190:193], v[56:59]
	v_mfma_f32_16x16x32_bf16 v[44:47], v[144:147], v[198:201], v[44:47]
	v_mfma_f32_16x16x32_bf16 v[40:43], v[166:169], v[198:201], v[40:43]
	v_mfma_f32_16x16x32_bf16 v[28:31], v[144:147], v[206:209], v[28:31]
	v_mfma_f32_16x16x32_bf16 v[24:27], v[166:169], v[206:209], v[24:27]
	v_mfma_f32_16x16x32_bf16 v[12:15], v[144:147], v[214:217], v[12:15]
	v_mfma_f32_16x16x32_bf16 v[8:11], v[166:169], v[214:217], v[8:11]
	v_mfma_f32_16x16x32_bf16 v[60:63], v[162:165], v[194:197], v[60:63]
	v_mfma_f32_16x16x32_bf16 v[56:59], v[170:173], v[194:197], v[56:59]
	v_mfma_f32_16x16x32_bf16 v[44:47], v[162:165], v[202:205], v[44:47]
	v_mfma_f32_16x16x32_bf16 v[40:43], v[170:173], v[202:205], v[40:43]
	v_mfma_f32_16x16x32_bf16 v[28:31], v[162:165], v[210:213], v[28:31]
	v_mfma_f32_16x16x32_bf16 v[24:27], v[170:173], v[210:213], v[24:27]
	v_mfma_f32_16x16x32_bf16 v[12:15], v[162:165], v[218:221], v[12:15]
	v_mfma_f32_16x16x32_bf16 v[8:11], v[170:173], v[218:221], v[8:11]
	s_setprio 0
	s_setprio 1
	v_mfma_f32_16x16x32_bf16 v[52:55], v[174:177], v[190:193], v[52:55]
	v_mfma_f32_16x16x32_bf16 v[48:51], v[182:185], v[190:193], v[48:51]
	v_mfma_f32_16x16x32_bf16 v[36:39], v[174:177], v[198:201], v[36:39]
	v_mfma_f32_16x16x32_bf16 v[32:35], v[182:185], v[198:201], v[32:35]
	v_mfma_f32_16x16x32_bf16 v[20:23], v[174:177], v[206:209], v[20:23]
	v_mfma_f32_16x16x32_bf16 v[16:19], v[182:185], v[206:209], v[16:19]
	v_mfma_f32_16x16x32_bf16 v[4:7], v[174:177], v[214:217], v[4:7]
	v_mfma_f32_16x16x32_bf16 v[0:3], v[182:185], v[214:217], v[0:3]
	v_mfma_f32_16x16x32_bf16 v[52:55], v[178:181], v[194:197], v[52:55]
	v_mfma_f32_16x16x32_bf16 v[48:51], v[186:189], v[194:197], v[48:51]
	v_mfma_f32_16x16x32_bf16 v[36:39], v[178:181], v[202:205], v[36:39]
	v_mfma_f32_16x16x32_bf16 v[32:35], v[186:189], v[202:205], v[32:35]
	v_mfma_f32_16x16x32_bf16 v[20:23], v[178:181], v[210:213], v[20:23]
	v_mfma_f32_16x16x32_bf16 v[16:19], v[186:189], v[210:213], v[16:19]
	v_mfma_f32_16x16x32_bf16 v[4:7], v[178:181], v[218:221], v[4:7]
	v_mfma_f32_16x16x32_bf16 v[0:3], v[186:189], v[218:221], v[0:3]
	s_setprio 0
	s_barrier
	s_add_i32 s70, 0, 0x18000
	s_add_i32 s71, 0, 0x1c000
	v_add_u32_e32 v162, s70, v149
	v_add_u32_e32 v178, s71, v149
	ds_read_b128 v[144:147], v162
	ds_read_b128 v[162:165], v162 offset:1024
	ds_read_b128 v[166:169], v154
	ds_read_b128 v[170:173], v155
	ds_read_b128 v[174:177], v178
	ds_read_b128 v[178:181], v178 offset:1024
	ds_read_b128 v[182:185], v156
	ds_read_b128 v[186:189], v157
	s_add_u32 s30, s30, 0x40000
	s_addc_u32 s31, s31, 0
	s_mov_b32 m0, s42
	ds_read_b128 v[190:193], v161 offset:32768
	ds_read_b128 v[194:197], v161 offset:33792
	ds_read_b128 v[198:201], v161 offset:34816
	ds_read_b128 v[202:205], v161 offset:35840
	ds_read_b128 v[206:209], v161 offset:36864
	ds_read_b128 v[210:213], v161 offset:37888
	ds_read_b128 v[214:217], v161 offset:38912
	ds_read_b128 v[218:221], v161 offset:39936
	global_load_lds_dwordx4 v134, s[30:31]
	s_mov_b32 m0, s43
	s_nop 0
	global_load_lds_dwordx4 v130, s[30:31]
	s_waitcnt vmcnt(8)
	s_waitcnt lgkmcnt(0)
	s_barrier
	s_setprio 1
	s_waitcnt lgkmcnt(0)
	v_mfma_f32_16x16x32_bf16 v[124:127], v[144:147], v[190:193], v[124:127]
	v_mfma_f32_16x16x32_bf16 v[120:123], v[166:169], v[190:193], v[120:123]
	v_mfma_f32_16x16x32_bf16 v[108:111], v[144:147], v[198:201], v[108:111]
	v_mfma_f32_16x16x32_bf16 v[104:107], v[166:169], v[198:201], v[104:107]
	v_mfma_f32_16x16x32_bf16 v[92:95], v[144:147], v[206:209], v[92:95]
	v_mfma_f32_16x16x32_bf16 v[88:91], v[166:169], v[206:209], v[88:91]
	v_mfma_f32_16x16x32_bf16 v[76:79], v[144:147], v[214:217], v[76:79]
	v_mfma_f32_16x16x32_bf16 v[72:75], v[166:169], v[214:217], v[72:75]
	v_mfma_f32_16x16x32_bf16 v[124:127], v[162:165], v[194:197], v[124:127]
	v_mfma_f32_16x16x32_bf16 v[120:123], v[170:173], v[194:197], v[120:123]
	v_mfma_f32_16x16x32_bf16 v[108:111], v[162:165], v[202:205], v[108:111]
	v_mfma_f32_16x16x32_bf16 v[104:107], v[170:173], v[202:205], v[104:107]
	v_mfma_f32_16x16x32_bf16 v[92:95], v[162:165], v[210:213], v[92:95]
	v_mfma_f32_16x16x32_bf16 v[88:91], v[170:173], v[210:213], v[88:91]
	v_mfma_f32_16x16x32_bf16 v[76:79], v[162:165], v[218:221], v[76:79]
	v_mfma_f32_16x16x32_bf16 v[72:75], v[170:173], v[218:221], v[72:75]
	s_setprio 0
	s_setprio 1
	v_mfma_f32_16x16x32_bf16 v[116:119], v[174:177], v[190:193], v[116:119]
	v_mfma_f32_16x16x32_bf16 v[112:115], v[182:185], v[190:193], v[112:115]
	v_mfma_f32_16x16x32_bf16 v[100:103], v[174:177], v[198:201], v[100:103]
	v_mfma_f32_16x16x32_bf16 v[96:99], v[182:185], v[198:201], v[96:99]
	v_mfma_f32_16x16x32_bf16 v[84:87], v[174:177], v[206:209], v[84:87]
	v_mfma_f32_16x16x32_bf16 v[80:83], v[182:185], v[206:209], v[80:83]
	v_mfma_f32_16x16x32_bf16 v[68:71], v[174:177], v[214:217], v[68:71]
	v_mfma_f32_16x16x32_bf16 v[64:67], v[182:185], v[214:217], v[64:67]
	v_mfma_f32_16x16x32_bf16 v[116:119], v[178:181], v[194:197], v[116:119]
	v_mfma_f32_16x16x32_bf16 v[112:115], v[186:189], v[194:197], v[112:115]
	v_mfma_f32_16x16x32_bf16 v[100:103], v[178:181], v[202:205], v[100:103]
	v_mfma_f32_16x16x32_bf16 v[96:99], v[186:189], v[202:205], v[96:99]
	v_mfma_f32_16x16x32_bf16 v[84:87], v[178:181], v[210:213], v[84:87]
	v_mfma_f32_16x16x32_bf16 v[80:83], v[186:189], v[210:213], v[80:83]
	v_mfma_f32_16x16x32_bf16 v[68:71], v[178:181], v[218:221], v[68:71]
	v_mfma_f32_16x16x32_bf16 v[64:67], v[186:189], v[218:221], v[64:67]
	s_setprio 0
	s_barrier
	s_add_i32 m0, s70, s37
	v_lshl_add_u64 v[222:223], v[222:223], 0, s[14:15]
	s_add_u32 s28, s28, 0x40080
	ds_read_b128 v[190:193], v161 offset:49152
	ds_read_b128 v[194:197], v161 offset:50176
	ds_read_b128 v[198:201], v161 offset:51200
	ds_read_b128 v[202:205], v161 offset:52224
	ds_read_b128 v[206:209], v161 offset:53248
	ds_read_b128 v[210:213], v161 offset:54272
	ds_read_b128 v[214:217], v161 offset:55296
	ds_read_b128 v[218:221], v161 offset:56320
	global_load_lds_dwordx4 v[222:223], off
	v_lshl_add_u64 v[222:223], v[224:225], 0, s[14:15]
	s_mov_b32 m0, s45
	s_addc_u32 s29, s29, 0
	global_load_lds_dwordx4 v[222:223], off
	s_add_i32 m0, s71, s37
	s_nop 0
	s_nop 1
	global_load_lds_dwordx4 v132, s[28:29]
	s_mov_b32 m0, s46
	s_nop 0
	global_load_lds_dwordx4 v128, s[28:29]
	v_lshl_add_u64 v[222:223], v[226:227], 0, s[14:15]
	s_mov_b32 m0, s48
	s_nop 0
	global_load_lds_dwordx4 v[222:223], off
	v_lshl_add_u64 v[222:223], v[228:229], 0, s[14:15]
	s_mov_b32 m0, s49
	s_nop 0
	global_load_lds_dwordx4 v[222:223], off
	s_waitcnt vmcnt(8)
	s_waitcnt lgkmcnt(0)
	s_barrier
	s_setprio 1
	s_waitcnt lgkmcnt(0)
	v_mfma_f32_16x16x32_bf16 v[60:63], v[144:147], v[190:193], v[60:63]
	v_mfma_f32_16x16x32_bf16 v[56:59], v[166:169], v[190:193], v[56:59]
	v_mfma_f32_16x16x32_bf16 v[44:47], v[144:147], v[198:201], v[44:47]
	v_mfma_f32_16x16x32_bf16 v[40:43], v[166:169], v[198:201], v[40:43]
	v_mfma_f32_16x16x32_bf16 v[28:31], v[144:147], v[206:209], v[28:31]
	v_mfma_f32_16x16x32_bf16 v[24:27], v[166:169], v[206:209], v[24:27]
	v_mfma_f32_16x16x32_bf16 v[12:15], v[144:147], v[214:217], v[12:15]
	v_mfma_f32_16x16x32_bf16 v[8:11], v[166:169], v[214:217], v[8:11]
	v_mfma_f32_16x16x32_bf16 v[60:63], v[162:165], v[194:197], v[60:63]
	v_mfma_f32_16x16x32_bf16 v[56:59], v[170:173], v[194:197], v[56:59]
	v_mfma_f32_16x16x32_bf16 v[44:47], v[162:165], v[202:205], v[44:47]
	v_mfma_f32_16x16x32_bf16 v[40:43], v[170:173], v[202:205], v[40:43]
	v_mfma_f32_16x16x32_bf16 v[28:31], v[162:165], v[210:213], v[28:31]
	v_mfma_f32_16x16x32_bf16 v[24:27], v[170:173], v[210:213], v[24:27]
	v_mfma_f32_16x16x32_bf16 v[12:15], v[162:165], v[218:221], v[12:15]
	v_mfma_f32_16x16x32_bf16 v[8:11], v[170:173], v[218:221], v[8:11]
	s_setprio 0
	s_setprio 1
	v_mfma_f32_16x16x32_bf16 v[52:55], v[174:177], v[190:193], v[52:55]
	v_mfma_f32_16x16x32_bf16 v[48:51], v[182:185], v[190:193], v[48:51]
	v_mfma_f32_16x16x32_bf16 v[36:39], v[174:177], v[198:201], v[36:39]
	v_mfma_f32_16x16x32_bf16 v[32:35], v[182:185], v[198:201], v[32:35]
	v_mfma_f32_16x16x32_bf16 v[20:23], v[174:177], v[206:209], v[20:23]
	v_mfma_f32_16x16x32_bf16 v[16:19], v[182:185], v[206:209], v[16:19]
	v_mfma_f32_16x16x32_bf16 v[4:7], v[174:177], v[214:217], v[4:7]
	v_mfma_f32_16x16x32_bf16 v[0:3], v[182:185], v[214:217], v[0:3]
	v_mfma_f32_16x16x32_bf16 v[52:55], v[178:181], v[194:197], v[52:55]
	v_mfma_f32_16x16x32_bf16 v[48:51], v[186:189], v[194:197], v[48:51]
	v_mfma_f32_16x16x32_bf16 v[36:39], v[178:181], v[202:205], v[36:39]
	v_mfma_f32_16x16x32_bf16 v[32:35], v[186:189], v[202:205], v[32:35]
	v_mfma_f32_16x16x32_bf16 v[20:23], v[178:181], v[210:213], v[20:23]
	v_mfma_f32_16x16x32_bf16 v[16:19], v[186:189], v[210:213], v[16:19]
	v_mfma_f32_16x16x32_bf16 v[4:7], v[178:181], v[218:221], v[4:7]
	v_mfma_f32_16x16x32_bf16 v[0:3], v[186:189], v[218:221], v[0:3]
	s_setprio 0
	s_barrier
	s_add_i32 s61, s61, 2
	s_add_u32 s26, s26, 0x100
	s_addc_u32 s27, s27, 0
	s_add_u32 s59, s59, 0x100
	s_addc_u32 s60, s60, 0
	s_cmp_gt_u32 s61, 13
	s_cbranch_scc0 .LBB0_409
	s_and_b64 vcc, exec, s[12:13]
	s_cbranch_vccz .LBB0_412
	s_barrier
